# L2: first task peeled as in L1 (static first task, rowptr/self/index loads under staging)
# baseline (speedup 1.0000x reference)
_Z7k_layerILi2EEvPKDF16_PKiPKjS3_S3_S1_PKfPDF16_PhS3_S7_Pf:
	s_load_dwordx2 s[24:25], s[0:1], 0x58
	s_load_dwordx4 s[12:15], s[0:1], 0x0
	s_load_dwordx2 s[26:27], s[0:1], 0x10
	s_load_dwordx4 s[16:19], s[0:1], 0x48
	s_load_dwordx4 s[20:23], s[0:1], 0x28
	v_lshrrev_b32_e32 v2, 5, v0
	v_and_b32_e32 v4, 31, v0
	v_mul_u32_u24_e32 v3, 0x210, v2
	v_lshlrev_b32_e32 v5, 4, v4
	v_add3_u32 v4, v3, v5, 0
	v_lshl_or_b32 v2, v2, 9, v5
	v_mov_b32_e32 v3, 0
	v_or_b32_e32 v1, 0xfffffc00, v0
	s_waitcnt lgkmcnt(0)
	v_add_u32_e32 v3, 0x4000, v2
	v_lshlrev_b32_e32 v14, 4, v0
	v_add_u32_e32 v15, 0xffffff00, v14
	v_lshrrev_b32_e32 v21, 6, v0
	s_mov_b64 s[4:5], exec
	v_cmp_gt_u32_e32 vcc, 16, v0
	v_cmp_gt_u32_e64 s[40:41], 48, v0
	s_andn2_b64 s[8:9], s[40:41], vcc
	s_and_b64 exec, s[4:5], vcc
	global_load_dwordx4 v[16:19], v14, s[22:23]
	s_and_b64 exec, s[4:5], s[8:9]
	global_load_dwordx4 v[16:19], v15, s[18:19]
	s_mov_b64 exec, s[4:5]
	global_load_dwordx4 v[22:25], v2, s[20:21]
	global_load_dwordx4 v[26:29], v3, s[20:21]
	v_readfirstlane_b32 s38, v21
	v_mov_b32_e32 v20, v4
	v_cmp_eq_u32_e32 vcc, 0, v0
	s_and_saveexec_b64 s[6:7], vcc
	v_mov_b32_e32 v1, 0
	v_mov_b32_e32 v2, 16
	ds_write_b32 v1, v2 offset:52224
	s_mov_b64 exec, s[6:7]
	s_mul_i32 s20, s2, 0x186a0
	s_lshr_b32 s20, s20, 8
	s_add_i32 s3, s2, 1
	s_mul_i32 s28, s3, 0x186a0
	s_lshr_b32 s28, s28, 8
.LBB5_10:
	v_lshrrev_b32_e32 v2, 3, v0
	s_load_dwordx2 s[30:31], s[0:1], 0x40
	v_and_b32_e32 v1, 63, v0
	v_and_b32_e32 v2, 0x78, v2
	s_movk_i32 s2, 0x90
	v_bfe_u32 v74, v0, 3, 3
	v_and_b32_e32 v75, 7, v0
	v_and_b32_e32 v77, 15, v0
	s_sub_i32 s0, s28, s20
	v_and_b32_e32 v5, 48, v0
	v_lshrrev_b32_e32 v0, 2, v0
	v_mad_u32_u24 v2, v2, s2, 0
	s_add_i32 s0, s0, 7
	v_mul_u32_u24_e32 v4, 0x90, v75
	v_and_b32_e32 v0, 12, v0
	v_lshlrev_b32_e32 v76, 4, v75
	s_ashr_i32 s21, s0, 3
	v_cmp_eq_u32_e64 s[0:1], 0, v1
	v_mad_u32_u24 v3, v74, s2, v2
	v_add3_u32 v80, v2, v4, v5
	v_add_u32_e32 v2, 0, v5
	v_cmp_gt_u32_e64 s[4:5], 16, v1
	v_mul_u32_u24_e32 v1, 0x210, v77
	v_lshlrev_b32_e32 v32, 2, v0
	v_mbcnt_lo_u32_b32 v0, -1, 0
	v_mov_b32_e32 v33, 0
	v_or_b32_e32 v78, 8, v75
	v_or_b32_e32 v79, 16, v75
	v_lshlrev_b32_e32 v81, 3, v75
	v_cmp_gt_u32_e64 s[2:3], 8, v77
	s_mov_b32 s29, 0x3c800000
	v_add_u32_e32 v82, v3, v76
	v_add_u32_e32 v83, v2, v1
	v_mbcnt_hi_u32_b32 v84, -1, v0
	s_lshl_b32 s33, s38, 3
	s_add_i32 s33, s33, s20
	v_add_u32_e32 v8, s33, v74
	v_cmp_gt_i32_e32 vcc, s28, v8
	v_mov_b32_e32 v0, 0
	v_mov_b32_e32 v1, 0
	v_mov_b32_e32 v2, 0
	v_mov_b32_e32 v3, 0
	v_mov_b32_e32 v4, 0
	v_mov_b32_e32 v5, 0
	v_mov_b32_e32 v6, 0
	v_mov_b32_e32 v7, 0
	s_and_saveexec_b64 s[6:7], vcc
	v_lshl_add_u32 v9, v8, 1, v8
	v_lshlrev_b32_e32 v9, 2, v9
	global_load_dwordx4 v[4:7], v9, s[14:15]
	v_lshl_or_b32 v9, v8, 7, v76
	global_load_dwordx4 v[0:3], v9, s[12:13]
	s_mov_b64 exec, s[6:7]
	s_waitcnt vmcnt(3)
	ds_write_b128 v20, v[22:25]
	s_waitcnt vmcnt(2)
	ds_write_b128 v20, v[26:29] offset:16896
	s_and_saveexec_b64 s[6:7], s[40:41]
	ds_write_b128 v14, v[16:19] offset:52240
	s_mov_b64 exec, s[6:7]
	s_waitcnt vmcnt(1)
	v_sub_u32_e32 v58, v5, v4
	v_sub_u32_e32 v87, v6, v5
	v_sub_u32_e32 v85, v7, v6
	v_add_lshl_u32 v10, v4, v75, 2
	v_add_lshl_u32 v11, v5, v75, 2
	v_add_lshl_u32 v12, v6, v75, 2
	v_mov_b32_e32 v9, 0x186a0
	v_mov_b32_e32 v8, 0x186a0
	v_mov_b32_e32 v60, 0x186a0
	v_mov_b32_e32 v59, 0x186a0
	v_mov_b32_e32 v62, 0x186a0
	v_mov_b32_e32 v89, 0x186a0
	v_mov_b32_e32 v88, 0x186a0
	v_mov_b32_e32 v86, 0x186a0
	v_mov_b32_e32 v7, 0x186a0
	s_mov_b64 s[6:7], exec
	v_cmp_lt_i32_e32 vcc, v75, v58
	s_and_b64 exec, exec, vcc
	global_load_dword v9, v10, s[26:27]
	v_cmp_lt_i32_e32 vcc, v78, v58
	s_and_b64 exec, exec, vcc
	global_load_dword v8, v10, s[26:27] offset:32
	v_cmp_lt_i32_e32 vcc, v79, v58
	s_and_b64 exec, exec, vcc
	global_load_dword v60, v10, s[26:27] offset:64
	s_mov_b64 exec, s[6:7]
	v_cmp_lt_i32_e32 vcc, v75, v87
	s_and_b64 exec, exec, vcc
	global_load_dword v59, v11, s[26:27]
	v_cmp_lt_i32_e32 vcc, v78, v87
	s_and_b64 exec, exec, vcc
	global_load_dword v62, v11, s[26:27] offset:32
	v_cmp_lt_i32_e32 vcc, v79, v87
	s_and_b64 exec, exec, vcc
	global_load_dword v89, v11, s[26:27] offset:64
	s_mov_b64 exec, s[6:7]
	v_cmp_lt_i32_e32 vcc, v75, v85
	s_and_b64 exec, exec, vcc
	global_load_dword v88, v12, s[26:27]
	v_cmp_lt_i32_e32 vcc, v78, v85
	s_and_b64 exec, exec, vcc
	global_load_dword v86, v12, s[26:27] offset:32
	v_cmp_lt_i32_e32 vcc, v79, v85
	s_and_b64 exec, exec, vcc
	global_load_dword v7, v12, s[26:27] offset:64
	s_mov_b64 exec, s[6:7]
	s_waitcnt lgkmcnt(0)
	s_barrier
	s_cmp_ge_i32 s38, s21
	s_cbranch_scc1 .LBB5_118
	s_branch .Lp2_after_idx

.Lp2_after_idx:
	s_waitcnt vmcnt(0)
	v_lshlrev_b32_e32 v9, 6, v9
	v_lshlrev_b32_e32 v8, 6, v8
	v_lshlrev_b32_e32 v60, 6, v60
	v_lshlrev_b32_e32 v59, 6, v59
	v_lshlrev_b32_e32 v62, 6, v62
	v_lshlrev_b32_e32 v89, 6, v89
	v_lshlrev_b32_e32 v88, 6, v88
	v_lshlrev_b32_e32 v86, 6, v86
	v_lshlrev_b32_e32 v7, 6, v7
	v_and_b32_e32 v9, 0x7fffc0, v9
	v_and_b32_e32 v8, 0x7fffc0, v8
	v_and_b32_e32 v60, 0x7fffc0, v60
	v_and_b32_e32 v59, 0x7fffc0, v59
	v_and_b32_e32 v62, 0x7fffc0, v62
	v_and_b32_e32 v89, 0x7fffc0, v89
	v_and_b32_e32 v88, 0x7fffc0, v88
	v_and_b32_e32 v86, 0x7fffc0, v86
	v_and_b32_e32 v7, 0x7fffc0, v7
	ds_swizzle_b32 v10, v9 offset:swizzle(BROADCAST,8,0)
	ds_swizzle_b32 v11, v9 offset:swizzle(BROADCAST,8,1)
	ds_swizzle_b32 v13, v9 offset:swizzle(BROADCAST,8,3)
	ds_swizzle_b32 v12, v9 offset:swizzle(BROADCAST,8,2)
	ds_swizzle_b32 v14, v9 offset:swizzle(BROADCAST,8,4)
	ds_swizzle_b32 v15, v9 offset:swizzle(BROADCAST,8,5)
	s_waitcnt lgkmcnt(0)
	v_add_u32_e32 v10, v10, v81
	v_add_u32_e32 v11, v11, v81
	v_add_u32_e32 v13, v13, v81
	ds_swizzle_b32 v16, v9 offset:swizzle(BROADCAST,8,6)
	ds_swizzle_b32 v9, v9 offset:swizzle(BROADCAST,8,7)
	v_add_u32_e32 v12, v12, v81
	global_load_dwordx2 v[56:57], v10, s[30:31]
	global_load_dwordx2 v[52:53], v11, s[30:31]
	global_load_dwordx2 v[30:31], v12, s[30:31]
	global_load_dwordx2 v[24:25], v13, s[30:31]
	v_add_u32_e32 v10, v14, v81
	v_add_u32_e32 v11, v15, v81
	ds_swizzle_b32 v13, v8 offset:swizzle(BROADCAST,8,0)
	ds_swizzle_b32 v14, v8 offset:swizzle(BROADCAST,8,1)
	ds_swizzle_b32 v15, v8 offset:swizzle(BROADCAST,8,2)
	s_waitcnt lgkmcnt(3)
	v_add_u32_e32 v9, v9, v81
	v_add_u32_e32 v12, v16, v81
	ds_swizzle_b32 v16, v8 offset:swizzle(BROADCAST,8,3)
	global_load_dwordx2 v[54:55], v10, s[30:31]
	global_load_dwordx2 v[50:51], v11, s[30:31]
	global_load_dwordx2 v[26:27], v12, s[30:31]
	global_load_dwordx2 v[20:21], v9, s[30:31]
	s_waitcnt lgkmcnt(3)
	v_add_u32_e32 v9, v13, v81
	s_waitcnt lgkmcnt(2)
	v_add_u32_e32 v10, v14, v81
	s_waitcnt lgkmcnt(1)
	v_add_u32_e32 v11, v15, v81
	ds_swizzle_b32 v13, v8 offset:swizzle(BROADCAST,8,4)
	ds_swizzle_b32 v14, v8 offset:swizzle(BROADCAST,8,5)
	ds_swizzle_b32 v15, v8 offset:swizzle(BROADCAST,8,6)
	ds_swizzle_b32 v8, v8 offset:swizzle(BROADCAST,8,7)
	s_waitcnt lgkmcnt(4)
	v_add_u32_e32 v12, v16, v81
	global_load_dwordx2 v[28:29], v9, s[30:31]
	global_load_dwordx2 v[22:23], v10, s[30:31]
	global_load_dwordx2 v[18:19], v11, s[30:31]
	global_load_dwordx2 v[16:17], v12, s[30:31]
	s_waitcnt lgkmcnt(3)
	v_add_u32_e32 v9, v13, v81
	s_waitcnt lgkmcnt(2)
	v_add_u32_e32 v10, v14, v81
	s_waitcnt lgkmcnt(1)
	v_add_u32_e32 v11, v15, v81
	s_waitcnt lgkmcnt(0)
	v_add_u32_e32 v8, v8, v81
	global_load_dwordx2 v[14:15], v9, s[30:31]
	global_load_dwordx2 v[12:13], v10, s[30:31]
	s_nop 0
	global_load_dwordx2 v[10:11], v11, s[30:31]
	s_nop 0
	global_load_dwordx2 v[8:9], v8, s[30:31]
	v_cmp_lt_i32_e32 vcc, 16, v58
	s_cmp_lg_u64 vcc, 0
	s_cselect_b64 s[36:37], -1, 0
	v_cmp_lt_i32_e64 s[10:11], 18, v58
	v_cmp_lt_i32_e64 s[8:9], 20, v58
	v_cmp_lt_i32_e64 s[6:7], 22, v58
	s_cbranch_vccz .LBB5_42
	ds_swizzle_b32 v34, v60 offset:swizzle(BROADCAST,8,0)
	ds_swizzle_b32 v35, v60 offset:swizzle(BROADCAST,8,1)
	s_waitcnt lgkmcnt(1)
	v_add_u32_e32 v34, v34, v81
	s_waitcnt lgkmcnt(0)
	v_add_u32_e32 v38, v35, v81
	global_load_dwordx2 v[34:35], v34, s[30:31]
	s_nop 0
	global_load_dwordx2 v[38:39], v38, s[30:31]

	.amdhsa_kernel _Z7k_layerILi2EEvPKDF16_PKiPKjS3_S3_S1_PKfPDF16_PhS3_S7_Pf
		.amdhsa_group_segment_fixed_size 768
		.amdhsa_private_segment_fixed_size 0
		.amdhsa_kernarg_size 352
		.amdhsa_user_sgpr_count 2
		.amdhsa_user_sgpr_dispatch_ptr 0
		.amdhsa_user_sgpr_queue_ptr 0
		.amdhsa_user_sgpr_kernarg_segment_ptr 1
		.amdhsa_user_sgpr_dispatch_id 0
		.amdhsa_user_sgpr_kernarg_preload_length 0
		.amdhsa_user_sgpr_kernarg_preload_offset 0
		.amdhsa_user_sgpr_private_segment_size 0
		.amdhsa_uses_dynamic_stack 0
		.amdhsa_enable_private_segment 0
		.amdhsa_system_sgpr_workgroup_id_x 1
		.amdhsa_system_sgpr_workgroup_id_y 0
		.amdhsa_system_sgpr_workgroup_id_z 0
		.amdhsa_system_sgpr_workgroup_info 0
		.amdhsa_system_vgpr_workitem_id 0
		.amdhsa_next_free_vgpr 102
		.amdhsa_next_free_sgpr 42
		.amdhsa_accum_offset 104
		.amdhsa_reserve_vcc 1
		.amdhsa_float_round_mode_32 0
		.amdhsa_float_round_mode_16_64 0
		.amdhsa_float_denorm_mode_32 3
		.amdhsa_float_denorm_mode_16_64 3
		.amdhsa_dx10_clamp 1
		.amdhsa_ieee_mode 1
		.amdhsa_fp16_overflow 0
		.amdhsa_tg_split 0
		.amdhsa_exception_fp_ieee_invalid_op 0
		.amdhsa_exception_fp_denorm_src 0
		.amdhsa_exception_fp_ieee_div_zero 0
		.amdhsa_exception_fp_ieee_overflow 0
		.amdhsa_exception_fp_ieee_underflow 0
		.amdhsa_exception_fp_ieee_inexact 0
		.amdhsa_exception_int_div_zero 0
	.end_amdhsa_kernel

amdhsa.kernels:
  - .agpr_count:     0
    .args:
      - .actual_access:  read_only
        .address_space:  global
        .offset:         0
        .size:           8
        .value_kind:     global_buffer
      - .actual_access:  read_only
        .address_space:  global
        .offset:         8
        .size:           8
        .value_kind:     global_buffer
      - .actual_access:  read_only
        .address_space:  global
        .offset:         16
        .size:           8
        .value_kind:     global_buffer
      - .actual_access:  read_only
        .address_space:  global
        .offset:         24
        .size:           8
        .value_kind:     global_buffer
      - .actual_access:  read_only
        .address_space:  global
        .offset:         32
        .size:           8
        .value_kind:     global_buffer
      - .actual_access:  read_only
        .address_space:  global
        .offset:         40
        .size:           8
        .value_kind:     global_buffer
      - .actual_access:  read_only
        .address_space:  global
        .offset:         48
        .size:           8
        .value_kind:     global_buffer
      - .actual_access:  read_only
        .address_space:  global
        .offset:         56
        .size:           8
        .value_kind:     global_buffer
      - .actual_access:  read_only
        .address_space:  global
        .offset:         64
        .size:           8
        .value_kind:     global_buffer
      - .actual_access:  read_only
        .address_space:  global
        .offset:         72
        .size:           8
        .value_kind:     global_buffer
      - .actual_access:  read_only
        .address_space:  global
        .offset:         80
        .size:           8
        .value_kind:     global_buffer
      - .actual_access:  read_only
        .address_space:  global
        .offset:         88
        .size:           8
        .value_kind:     global_buffer
      - .actual_access:  write_only
        .address_space:  global
        .offset:         96
        .size:           8
        .value_kind:     global_buffer
      - .actual_access:  write_only
        .address_space:  global
        .offset:         104
        .size:           8
        .value_kind:     global_buffer
      - .actual_access:  write_only
        .address_space:  global
        .offset:         112
        .size:           8
        .value_kind:     global_buffer
      - .actual_access:  write_only
        .address_space:  global
        .offset:         120
        .size:           8
        .value_kind:     global_buffer
      - .actual_access:  write_only
        .address_space:  global
        .offset:         128
        .size:           8
        .value_kind:     global_buffer
      - .actual_access:  write_only
        .address_space:  global
        .offset:         136
        .size:           8
        .value_kind:     global_buffer
      - .actual_access:  write_only
        .address_space:  global
        .offset:         144
        .size:           8
        .value_kind:     global_buffer
      - .actual_access:  write_only
        .address_space:  global
        .offset:         152
        .size:           8
        .value_kind:     global_buffer
      - .actual_access:  write_only
        .address_space:  global
        .offset:         160
        .size:           8
        .value_kind:     global_buffer
    .group_segment_fixed_size: 0
    .kernarg_segment_align: 8
    .kernarg_segment_size: 168
    .language:       OpenCL C
    .language_version:
      - 2
      - 0
    .max_flat_workgroup_size: 1024
    .name:           _Z6k_prepPKiS0_PKfS2_S2_S2_S2_S2_S2_S2_S2_S2_PDF16_S3_S3_PfS4_S4_PjS3_S5_
    .private_segment_fixed_size: 0
    .sgpr_count:     27
    .sgpr_spill_count: 0
    .symbol:         _Z6k_prepPKiS0_PKfS2_S2_S2_S2_S2_S2_S2_S2_S2_PDF16_S3_S3_PfS4_S4_PjS3_S5_.kd
    .uniform_work_group_size: 1
    .uses_dynamic_stack: false
    .vgpr_count:     61
    .vgpr_spill_count: 0
    .wavefront_size: 64
  - .agpr_count:     0
    .args:
      - .actual_access:  read_only
        .address_space:  global
        .offset:         0
        .size:           8
        .value_kind:     global_buffer
      - .actual_access:  read_only
        .address_space:  global
        .offset:         8
        .size:           8
        .value_kind:     global_buffer
      - .actual_access:  read_only
        .address_space:  global
        .offset:         16
        .size:           8
        .value_kind:     global_buffer
      - .actual_access:  write_only
        .address_space:  global
        .offset:         24
        .size:           8
        .value_kind:     global_buffer
      - .actual_access:  write_only
        .address_space:  global
        .offset:         32
        .size:           8
        .value_kind:     global_buffer
      - .actual_access:  write_only
        .address_space:  global
        .offset:         40
        .size:           8
        .value_kind:     global_buffer
      - .actual_access:  read_only
        .address_space:  global
        .offset:         48
        .size:           8
        .value_kind:     global_buffer
      - .actual_access:  read_only
        .address_space:  global
        .offset:         56
        .size:           8
        .value_kind:     global_buffer
      - .actual_access:  read_only
        .address_space:  global
        .offset:         64
        .size:           8
        .value_kind:     global_buffer
      - .actual_access:  read_only
        .address_space:  global
        .offset:         72
        .size:           8
        .value_kind:     global_buffer
      - .actual_access:  read_only
        .address_space:  global
        .offset:         80
        .size:           8
        .value_kind:     global_buffer
      - .actual_access:  read_only
        .address_space:  global
        .offset:         88
        .size:           8
        .value_kind:     global_buffer
      - .actual_access:  read_only
        .address_space:  global
        .offset:         96
        .size:           8
        .value_kind:     global_buffer
      - .actual_access:  read_only
        .address_space:  global
        .offset:         104
        .size:           8
        .value_kind:     global_buffer
      - .actual_access:  read_only
        .address_space:  global
        .offset:         112
        .size:           8
        .value_kind:     global_buffer
      - .actual_access:  read_only
        .address_space:  global
        .offset:         120
        .size:           8
        .value_kind:     global_buffer
      - .actual_access:  read_only
        .address_space:  global
        .offset:         128
        .size:           8
        .value_kind:     global_buffer
      - .actual_access:  write_only
        .address_space:  global
        .offset:         136
        .size:           8
        .value_kind:     global_buffer
      - .actual_access:  write_only
        .address_space:  global
        .offset:         144
        .size:           8
        .value_kind:     global_buffer
      - .actual_access:  write_only
        .address_space:  global
        .offset:         152
        .size:           8
        .value_kind:     global_buffer
      - .actual_access:  write_only
        .address_space:  global
        .offset:         160
        .size:           8
        .value_kind:     global_buffer
      - .actual_access:  write_only
        .address_space:  global
        .offset:         168
        .size:           8
        .value_kind:     global_buffer
    .group_segment_fixed_size: 1696
    .kernarg_segment_align: 8
    .kernarg_segment_size: 176
    .language:       OpenCL C
    .language_version:
      - 2
      - 0
    .max_flat_workgroup_size: 1024
    .name:           _Z11k_localsortPKiS0_S0_PjPtPiPKjPKfS7_S7_S7_S7_S7_S7_S7_S7_S7_PDF16_S8_S8_PfS9_
    .private_segment_fixed_size: 0
    .sgpr_count:     71
    .sgpr_spill_count: 0
    .symbol:         _Z11k_localsortPKiS0_S0_PjPtPiPKjPKfS7_S7_S7_S7_S7_S7_S7_S7_S7_PDF16_S8_S8_PfS9_.kd
    .uniform_work_group_size: 1
    .uses_dynamic_stack: false
    .vgpr_count:     95
    .vgpr_spill_count: 0
    .wavefront_size: 64
  - .agpr_count:     0
    .args:
      - .actual_access:  read_only
        .address_space:  global
        .offset:         0
        .size:           8
        .value_kind:     global_buffer
      - .actual_access:  read_only
        .address_space:  global
        .offset:         8
        .size:           8
        .value_kind:     global_buffer
      - .actual_access:  read_only
        .address_space:  global
        .offset:         16
        .size:           8
        .value_kind:     global_buffer
      - .actual_access:  write_only
        .address_space:  global
        .offset:         24
        .size:           8
        .value_kind:     global_buffer
      - .actual_access:  write_only
        .address_space:  global
        .offset:         32
        .size:           8
        .value_kind:     global_buffer
    .group_segment_fixed_size: 54144
    .kernarg_segment_align: 8
    .kernarg_segment_size: 40
    .language:       OpenCL C
    .language_version:
      - 2
      - 0
    .max_flat_workgroup_size: 1024
    .name:           _Z12k_bucketsortPKjPKtPKiPiPj
    .private_segment_fixed_size: 0
    .sgpr_count:     70
    .sgpr_spill_count: 0
    .symbol:         _Z12k_bucketsortPKjPKtPKiPiPj.kd
    .uniform_work_group_size: 1
    .uses_dynamic_stack: false
    .vgpr_count:     59
    .vgpr_spill_count: 0
    .wavefront_size: 64
  - .agpr_count:     0
    .args:
      - .actual_access:  read_only
        .address_space:  global
        .offset:         0
        .size:           8
        .value_kind:     global_buffer
      - .actual_access:  read_only
        .address_space:  global
        .offset:         8
        .size:           8
        .value_kind:     global_buffer
      - .actual_access:  write_only
        .address_space:  global
        .offset:         16
        .size:           8
        .value_kind:     global_buffer
    .group_segment_fixed_size: 0
    .kernarg_segment_align: 8
    .kernarg_segment_size: 24
    .language:       OpenCL C
    .language_version:
      - 2
      - 0
    .max_flat_workgroup_size: 256
    .name:           _Z7k_finalPKfS0_Pf
    .private_segment_fixed_size: 0
    .sgpr_count:     14
    .sgpr_spill_count: 0
    .symbol:         _Z7k_finalPKfS0_Pf.kd
    .uniform_work_group_size: 1
    .uses_dynamic_stack: false
    .vgpr_count:     10
    .vgpr_spill_count: 0
    .wavefront_size: 64
  - .agpr_count:     0
    .args:
      - .actual_access:  read_only
        .address_space:  global
        .offset:         0
        .size:           8
        .value_kind:     global_buffer
      - .actual_access:  read_only
        .address_space:  global
        .offset:         8
        .size:           8
        .value_kind:     global_buffer
      - .actual_access:  read_only
        .address_space:  global
        .offset:         16
        .size:           8
        .value_kind:     global_buffer
      - .actual_access:  read_only
        .address_space:  global
        .offset:         24
        .size:           8
        .value_kind:     global_buffer
      - .actual_access:  read_only
        .address_space:  global
        .offset:         32
        .size:           8
        .value_kind:     global_buffer
      - .actual_access:  read_only
        .address_space:  global
        .offset:         40
        .size:           8
        .value_kind:     global_buffer
      - .address_space:  global
        .offset:         48
        .size:           8
        .value_kind:     global_buffer
      - .actual_access:  write_only
        .address_space:  global
        .offset:         56
        .size:           8
        .value_kind:     global_buffer
      - .address_space:  global
        .offset:         64
        .size:           8
        .value_kind:     global_buffer
      - .actual_access:  read_only
        .address_space:  global
        .offset:         72
        .size:           8
        .value_kind:     global_buffer
      - .address_space:  global
        .offset:         80
        .size:           8
        .value_kind:     global_buffer
      - .actual_access:  read_only
        .address_space:  global
        .offset:         88
        .size:           8
        .value_kind:     global_buffer
      - .offset:         96
        .size:           4
        .value_kind:     hidden_block_count_x
      - .offset:         100
        .size:           4
        .value_kind:     hidden_block_count_y
      - .offset:         104
        .size:           4
        .value_kind:     hidden_block_count_z
      - .offset:         108
        .size:           2
        .value_kind:     hidden_group_size_x
      - .offset:         110
        .size:           2
        .value_kind:     hidden_group_size_y
      - .offset:         112
        .size:           2
        .value_kind:     hidden_group_size_z
      - .offset:         114
        .size:           2
        .value_kind:     hidden_remainder_x
      - .offset:         116
        .size:           2
        .value_kind:     hidden_remainder_y
      - .offset:         118
        .size:           2
        .value_kind:     hidden_remainder_z
      - .offset:         136
        .size:           8
        .value_kind:     hidden_global_offset_x
      - .offset:         144
        .size:           8
        .value_kind:     hidden_global_offset_y
      - .offset:         152
        .size:           8
        .value_kind:     hidden_global_offset_z
      - .offset:         160
        .size:           2
        .value_kind:     hidden_grid_dims
      - .offset:         216
        .size:           4
        .value_kind:     hidden_dynamic_lds_size
    .group_segment_fixed_size: 256
    .kernarg_segment_align: 8
    .kernarg_segment_size: 352
    .language:       OpenCL C
    .language_version:
      - 2
      - 0
    .max_flat_workgroup_size: 1024
    .name:           _Z7k_layerILi1EEvPKDF16_PKiPKjS3_S3_S1_PKfPDF16_PhS3_S7_Pf
    .private_segment_fixed_size: 0
    .sgpr_count:     43
    .sgpr_spill_count: 0
    .symbol:         _Z7k_layerILi1EEvPKDF16_PKiPKjS3_S3_S1_PKfPDF16_PhS3_S7_Pf.kd
    .uniform_work_group_size: 1
    .uses_dynamic_stack: false
    .vgpr_count:     114
    .vgpr_spill_count: 0
    .wavefront_size: 64
  - .agpr_count:     0
    .args:
      - .actual_access:  read_only
        .address_space:  global
        .offset:         0
        .size:           8
        .value_kind:     global_buffer
      - .actual_access:  read_only
        .address_space:  global
        .offset:         8
        .size:           8
        .value_kind:     global_buffer
      - .actual_access:  read_only
        .address_space:  global
        .offset:         16
        .size:           8
        .value_kind:     global_buffer
      - .actual_access:  read_only
        .address_space:  global
        .offset:         24
        .size:           8
        .value_kind:     global_buffer
      - .actual_access:  read_only
        .address_space:  global
        .offset:         32
        .size:           8
        .value_kind:     global_buffer
      - .actual_access:  read_only
        .address_space:  global
        .offset:         40
        .size:           8
        .value_kind:     global_buffer
      - .address_space:  global
        .offset:         48
        .size:           8
        .value_kind:     global_buffer
      - .actual_access:  read_only
        .address_space:  global
        .offset:         56
        .size:           8
        .value_kind:     global_buffer
      - .address_space:  global
        .offset:         64
        .size:           8
        .value_kind:     global_buffer
      - .actual_access:  read_only
        .address_space:  global
        .offset:         72
        .size:           8
        .value_kind:     global_buffer
      - .address_space:  global
        .offset:         80
        .size:           8
        .value_kind:     global_buffer
      - .address_space:  global
        .offset:         88
        .size:           8
        .value_kind:     global_buffer
      - .offset:         96
        .size:           4
        .value_kind:     hidden_block_count_x
      - .offset:         100
        .size:           4
        .value_kind:     hidden_block_count_y
      - .offset:         104
        .size:           4
        .value_kind:     hidden_block_count_z
      - .offset:         108
        .size:           2
        .value_kind:     hidden_group_size_x
      - .offset:         110
        .size:           2
        .value_kind:     hidden_group_size_y
      - .offset:         112
        .size:           2
        .value_kind:     hidden_group_size_z
      - .offset:         114
        .size:           2
        .value_kind:     hidden_remainder_x
      - .offset:         116
        .size:           2
        .value_kind:     hidden_remainder_y
      - .offset:         118
        .size:           2
        .value_kind:     hidden_remainder_z
      - .offset:         136
        .size:           8
        .value_kind:     hidden_global_offset_x
      - .offset:         144
        .size:           8
        .value_kind:     hidden_global_offset_y
      - .offset:         152
        .size:           8
        .value_kind:     hidden_global_offset_z
      - .offset:         160
        .size:           2
        .value_kind:     hidden_grid_dims
      - .offset:         216
        .size:           4
        .value_kind:     hidden_dynamic_lds_size
    .group_segment_fixed_size: 768
    .kernarg_segment_align: 8
    .kernarg_segment_size: 352
    .language:       OpenCL C
    .language_version:
      - 2
      - 0
    .max_flat_workgroup_size: 1024
    .name:           _Z7k_layerILi2EEvPKDF16_PKiPKjS3_S3_S1_PKfPDF16_PhS3_S7_Pf
    .private_segment_fixed_size: 0
    .sgpr_count:     48
    .sgpr_spill_count: 0
    .symbol:         _Z7k_layerILi2EEvPKDF16_PKiPKjS3_S3_S1_PKfPDF16_PhS3_S7_Pf.kd
    .uniform_work_group_size: 1
    .uses_dynamic_stack: false
    .vgpr_count:     102
    .vgpr_spill_count: 0
    .wavefront_size: 64
